# speedup vs baseline: 1.0104x; 1.0104x over previous
.Lk2f_b2:
	s_waitcnt lgkmcnt(0)
	s_barrier
	v_and_b32_e32 v1, 63, v0
	v_lshlrev_b32_e32 v6, 3, v1
	ds_read_b64 v[14:15], v6 offset:18688
	s_cmp_eq_u32 s4, 7
	s_cbranch_scc1 .Lk2f_w7
	v_lshrrev_b32_e32 v3, 2, v1
	s_mul_i32 s5, s4, 14
	v_add_u32_e32 v6, s5, v3
	v_cmp_gt_u32_e32 vcc, 14, v3
	v_mov_b32_e32 v7, 0x7f
	v_mov_b32_e32 v8, 0x62
	v_and_b32_e32 v9, 3, v1
	v_cndmask_b32_e32 v7, v7, v6, vcc
	v_cndmask_b32_e32 v8, v8, v6, vcc
	v_lshlrev_b32_e32 v7, 2, v7
	v_mul_u32_u24_e32 v2, 0x90, v8
	ds_read_b32 v3, v7 offset:18688
	ds_read_b128 v[4:7], v2 offset:19456
	v_lshlrev_b32_e32 v1, 4, v9
	s_mov_b32 s32, s8
	s_and_b32 s33, s9, 0xffff
	s_mov_b32 s34, 0xc35000
	s_mov_b32 s35, 0x20000
	v_and_b32_e32 v8, 15, v0
	v_add_u32_e32 v9, s5, v8
	s_mul_i32 s6, s3, 0x62
	v_add_u32_e32 v9, s6, v9
	v_cmp_gt_u32_e32 vcc, 14, v8
	s_mov_b32 s7, 0x186a0
	v_cmp_gt_u32_e64 s[38:39], s7, v9
	s_and_b64 vcc, vcc, s[38:39]
	s_mov_b64 s[40:41], vcc
	v_and_b32_e32 v8, 0x30, v0
	v_cndmask_b32_e32 v9, 0, v9, vcc
	v_lshl_or_b32 v56, v9, 7, v8
	v_mov_b32_e32 v40, 0
	v_mov_b32_e32 v41, 0
	v_mov_b32_e32 v42, 0
	v_mov_b32_e32 v43, 0
	v_mov_b32_e32 v44, 0
	v_mov_b32_e32 v45, 0
	v_mov_b32_e32 v46, 0
	v_mov_b32_e32 v47, 0
	v_mov_b32_e32 v48, 0
	v_mov_b32_e32 v49, 0
	v_mov_b32_e32 v50, 0
	v_mov_b32_e32 v51, 0
	v_mov_b32_e32 v52, 0
	v_mov_b32_e32 v53, 0
	v_mov_b32_e32 v54, 0
	v_mov_b32_e32 v55, 0
	s_mov_b32 s5, 0
	s_waitcnt lgkmcnt(0)
	v_max_u32_e32 v8, v14, v15
	v_cmp_lt_u32_e32 vcc, 32, v8
	s_cmp_lg_u64 vcc, 0
	s_cbranch_scc1 .Lk2f_fallback
	v_cmp_lt_i32_e32 vcc, 0, v3
	s_cmp_lg_u64 vcc, 0
	s_cbranch_scc0 .Lk2f_gdone
.Lk2f_loop:
	v_lshl_or_b32 v4, v4, 7, v1
	v_lshl_or_b32 v5, v5, 7, v1
	v_lshl_or_b32 v6, v6, 7, v1
	v_lshl_or_b32 v7, v7, 7, v1
	buffer_load_dwordx4 v[8:11], v4, s[32:35], 0 offen
	buffer_load_dwordx4 v[12:15], v4, s[32:35], 0 offen offset:64
	buffer_load_dwordx4 v[16:19], v5, s[32:35], 0 offen
	buffer_load_dwordx4 v[20:23], v5, s[32:35], 0 offen offset:64
	buffer_load_dwordx4 v[24:27], v6, s[32:35], 0 offen
	buffer_load_dwordx4 v[28:31], v6, s[32:35], 0 offen offset:64
	buffer_load_dwordx4 v[32:35], v7, s[32:35], 0 offen
	buffer_load_dwordx4 v[36:39], v7, s[32:35], 0 offen offset:64
	v_add_u32_e32 v2, 16, v2
	s_add_i32 s5, s5, 4
	ds_read_b128 v[4:7], v2 offset:19456
	v_cmp_lt_i32_e32 vcc, s5, v3
	s_waitcnt vmcnt(5)
	v_pk_add_f16 v8, v8, v16
	v_pk_add_f16 v9, v9, v17
	v_pk_add_f16 v10, v10, v18
	v_pk_add_f16 v11, v11, v19
	s_waitcnt vmcnt(4)
	v_pk_add_f16 v12, v12, v20
	v_pk_add_f16 v13, v13, v21
	v_pk_add_f16 v14, v14, v22
	v_pk_add_f16 v15, v15, v23
	s_waitcnt vmcnt(1)
	v_pk_add_f16 v24, v24, v32
	v_pk_add_f16 v25, v25, v33
	v_pk_add_f16 v26, v26, v34
	v_pk_add_f16 v27, v27, v35
	v_pk_add_f16 v8, v8, v24
	v_pk_add_f16 v9, v9, v25
	v_pk_add_f16 v10, v10, v26
	v_pk_add_f16 v11, v11, v27
	s_waitcnt vmcnt(0)
	v_pk_add_f16 v28, v28, v36
	v_pk_add_f16 v29, v29, v37
	v_pk_add_f16 v30, v30, v38
	v_pk_add_f16 v31, v31, v39
	v_pk_add_f16 v12, v12, v28
	v_pk_add_f16 v13, v13, v29
	v_pk_add_f16 v14, v14, v30
	v_pk_add_f16 v15, v15, v31
	v_fma_mix_f32 v40, v8, 1.0, v40 op_sel:[0,0,0] op_sel_hi:[1,0,0]
	v_fma_mix_f32 v41, v8, 1.0, v41 op_sel:[1,0,0] op_sel_hi:[1,0,0]
	v_fma_mix_f32 v42, v9, 1.0, v42 op_sel:[0,0,0] op_sel_hi:[1,0,0]
	v_fma_mix_f32 v43, v9, 1.0, v43 op_sel:[1,0,0] op_sel_hi:[1,0,0]
	v_fma_mix_f32 v44, v10, 1.0, v44 op_sel:[0,0,0] op_sel_hi:[1,0,0]
	v_fma_mix_f32 v45, v10, 1.0, v45 op_sel:[1,0,0] op_sel_hi:[1,0,0]
	v_fma_mix_f32 v46, v11, 1.0, v46 op_sel:[0,0,0] op_sel_hi:[1,0,0]
	v_fma_mix_f32 v47, v11, 1.0, v47 op_sel:[1,0,0] op_sel_hi:[1,0,0]
	v_fma_mix_f32 v48, v12, 1.0, v48 op_sel:[0,0,0] op_sel_hi:[1,0,0]
	v_fma_mix_f32 v49, v12, 1.0, v49 op_sel:[1,0,0] op_sel_hi:[1,0,0]
	v_fma_mix_f32 v50, v13, 1.0, v50 op_sel:[0,0,0] op_sel_hi:[1,0,0]
	v_fma_mix_f32 v51, v13, 1.0, v51 op_sel:[1,0,0] op_sel_hi:[1,0,0]
	v_fma_mix_f32 v52, v14, 1.0, v52 op_sel:[0,0,0] op_sel_hi:[1,0,0]
	v_fma_mix_f32 v53, v14, 1.0, v53 op_sel:[1,0,0] op_sel_hi:[1,0,0]
	v_fma_mix_f32 v54, v15, 1.0, v54 op_sel:[0,0,0] op_sel_hi:[1,0,0]
	v_fma_mix_f32 v55, v15, 1.0, v55 op_sel:[1,0,0] op_sel_hi:[1,0,0]
	s_cmp_lg_u32 s5, 4
	s_cbranch_scc1 .Lk2f_noself
	buffer_load_dwordx4 v[60:63], v56, s[32:35], 0 offen offset:64
	buffer_load_dwordx4 v[56:59], v56, s[32:35], 0 offen
.Lk2f_noself:
	s_waitcnt lgkmcnt(0)
	s_cmp_lg_u64 vcc, 0
	s_cbranch_scc1 .Lk2f_loop
	s_branch .Lk2f_gdone2
.Lk2f_gdone:
	buffer_load_dwordx4 v[60:63], v56, s[32:35], 0 offen offset:64
	buffer_load_dwordx4 v[56:59], v56, s[32:35], 0 offen
